# baseline (speedup 1.0000x reference)
.Lp_q:
	v_lshrrev_b32_e32 v122, 5, v0
	v_lshlrev_b32_e32 v122, 10, v122
	v_and_b32_e32 v125, 31, v0
	v_lshl_add_u32 v122, v125, 4, v122
	s_and_b32 s13, s2, 7
	s_lshl_b32 s14, s13, 14
	v_add_u32_e32 v125, s14, v122
	global_load_dwordx4 v[132:135], v125, s[28:29]
	s_add_i32 s13, s2, 1
	s_and_b32 s13, s13, 7
	s_lshl_b32 s14, s13, 14
	v_add_u32_e32 v125, s14, v122
	global_load_dwordx4 v[136:139], v125, s[28:29]
	s_add_i32 s13, s2, 2
	s_and_b32 s13, s13, 7
	s_lshl_b32 s14, s13, 14
	v_add_u32_e32 v125, s14, v122
	global_load_dwordx4 v[140:143], v125, s[28:29]
	s_add_i32 s13, s2, 3
	s_and_b32 s13, s13, 7
	s_lshl_b32 s14, s13, 14
	v_add_u32_e32 v125, s14, v122
	global_load_dwordx4 v[144:147], v125, s[28:29]
	s_add_i32 s13, s2, 4
	s_and_b32 s13, s13, 7
	s_lshl_b32 s14, s13, 14
	v_add_u32_e32 v125, s14, v122
	global_load_dwordx4 v[148:151], v125, s[28:29]
	s_add_i32 s13, s2, 5
	s_and_b32 s13, s13, 7
	s_lshl_b32 s14, s13, 14
	v_add_u32_e32 v125, s14, v122
	global_load_dwordx4 v[152:155], v125, s[28:29]
	s_add_i32 s13, s2, 6
	s_and_b32 s13, s13, 7
	s_lshl_b32 s14, s13, 14
	v_add_u32_e32 v125, s14, v122
	global_load_dwordx4 v[156:159], v125, s[28:29]
	s_add_i32 s13, s2, 7
	s_and_b32 s13, s13, 7
	s_lshl_b32 s14, s13, 14
	v_add_u32_e32 v125, s14, v122
	global_load_dwordx4 v[160:163], v125, s[28:29]
	s_waitcnt vmcnt(18)
	v_cvt_pk_bf16_f32 v12, v2, v3
	v_cvt_pk_bf16_f32 v13, v4, v5
	ds_write_b64 v124, v[12:13]
	s_waitcnt vmcnt(17)
	v_cvt_pk_bf16_f32 v6, v80, v81
	v_cvt_pk_bf16_f32 v7, v82, v83
	s_and_b32 s13, s2, 7
	s_mul_i32 s14, s13, 0x1100
	v_add_u32_e32 v125, s14, v58
	ds_write_b64 v125, v[6:7]
	s_waitcnt vmcnt(16)
	v_cvt_pk_bf16_f32 v8, v84, v85
	v_cvt_pk_bf16_f32 v9, v86, v87
	s_add_i32 s13, s2, 1
	s_and_b32 s13, s13, 7
	s_mul_i32 s14, s13, 0x1100
	v_add_u32_e32 v10, s14, v58
	ds_write_b64 v10, v[8:9]
	s_waitcnt vmcnt(15)
	v_cvt_pk_bf16_f32 v6, v88, v89
	v_cvt_pk_bf16_f32 v7, v90, v91
	s_add_i32 s13, s2, 2
	s_and_b32 s13, s13, 7
	s_mul_i32 s14, s13, 0x1100
	v_add_u32_e32 v125, s14, v58
	ds_write_b64 v125, v[6:7]
	s_waitcnt vmcnt(14)
	v_cvt_pk_bf16_f32 v8, v92, v93
	v_cvt_pk_bf16_f32 v9, v94, v95
	s_add_i32 s13, s2, 3
	s_and_b32 s13, s13, 7
	s_mul_i32 s14, s13, 0x1100
	v_add_u32_e32 v10, s14, v58
	ds_write_b64 v10, v[8:9]
	s_waitcnt vmcnt(13)
	v_cvt_pk_bf16_f32 v6, v96, v97
	v_cvt_pk_bf16_f32 v7, v98, v99
	s_add_i32 s13, s2, 4
	s_and_b32 s13, s13, 7
	s_mul_i32 s14, s13, 0x1100
	v_add_u32_e32 v125, s14, v58
	ds_write_b64 v125, v[6:7]
	s_waitcnt vmcnt(12)
	v_cvt_pk_bf16_f32 v8, v100, v101
	v_cvt_pk_bf16_f32 v9, v102, v103
	s_add_i32 s13, s2, 5
	s_and_b32 s13, s13, 7
	s_mul_i32 s14, s13, 0x1100
	v_add_u32_e32 v10, s14, v58
	ds_write_b64 v10, v[8:9]
	s_waitcnt vmcnt(11)
	v_cvt_pk_bf16_f32 v6, v108, v109
	v_cvt_pk_bf16_f32 v7, v110, v111
	s_add_i32 s13, s2, 6
	s_and_b32 s13, s13, 7
	s_mul_i32 s14, s13, 0x1100
	v_add_u32_e32 v125, s14, v58
	ds_write_b64 v125, v[6:7]
	s_waitcnt vmcnt(10)
	v_cvt_pk_bf16_f32 v8, v112, v113
	v_cvt_pk_bf16_f32 v9, v114, v115
	s_add_i32 s13, s2, 7
	s_and_b32 s13, s13, 7
	s_mul_i32 s14, s13, 0x1100
	v_add_u32_e32 v10, s14, v58
	ds_write_b64 v10, v[8:9]
	v_lshl_add_u32 v123, v128, 1, s12
	v_lshlrev_b32_e32 v123, 12, v123
	v_lshl_add_u32 v123, v126, 4, v123
	v_add_u32_e32 v121, 0x1000, v123
	global_load_dwordx4 v[164:167], v123, s[34:35] nt
	global_load_dwordx4 v[168:171], v123, s[34:35] offset:1024 nt
	global_load_dwordx4 v[172:175], v123, s[34:35] offset:2048 nt
	global_load_dwordx4 v[176:179], v123, s[34:35] offset:3072 nt
	global_load_dwordx4 v[180:183], v121, s[34:35] nt
	global_load_dwordx4 v[184:187], v121, s[34:35] offset:1024 nt
	global_load_dwordx4 v[188:191], v121, s[34:35] offset:2048 nt
	global_load_dwordx4 v[192:195], v121, s[34:35] offset:3072 nt
	s_waitcnt vmcnt(15)
	v_cvt_pk_bf16_f32 v6, v132, v133
	v_cvt_pk_bf16_f32 v7, v134, v135
	s_and_b32 s13, s2, 7
	s_mul_i32 s14, s13, 0x1100
	s_add_i32 s14, s14, 34816
	v_add_u32_e32 v125, s14, v58
	ds_write_b64 v125, v[6:7]
	s_waitcnt vmcnt(14)
	v_cvt_pk_bf16_f32 v8, v136, v137
	v_cvt_pk_bf16_f32 v9, v138, v139
	s_add_i32 s13, s2, 1
	s_and_b32 s13, s13, 7
	s_mul_i32 s14, s13, 0x1100
	s_add_i32 s14, s14, 34816
	v_add_u32_e32 v10, s14, v58
	ds_write_b64 v10, v[8:9]
	s_waitcnt vmcnt(13)
	v_cvt_pk_bf16_f32 v6, v140, v141
	v_cvt_pk_bf16_f32 v7, v142, v143
	s_add_i32 s13, s2, 2
	s_and_b32 s13, s13, 7
	s_mul_i32 s14, s13, 0x1100
	s_add_i32 s14, s14, 34816
	v_add_u32_e32 v125, s14, v58
	ds_write_b64 v125, v[6:7]
	s_waitcnt vmcnt(12)
	v_cvt_pk_bf16_f32 v8, v144, v145
	v_cvt_pk_bf16_f32 v9, v146, v147
	s_add_i32 s13, s2, 3
	s_and_b32 s13, s13, 7
	s_mul_i32 s14, s13, 0x1100
	s_add_i32 s14, s14, 34816
	v_add_u32_e32 v10, s14, v58
	ds_write_b64 v10, v[8:9]
	s_waitcnt vmcnt(11)
	v_cvt_pk_bf16_f32 v6, v148, v149
	v_cvt_pk_bf16_f32 v7, v150, v151
	s_add_i32 s13, s2, 4
	s_and_b32 s13, s13, 7
	s_mul_i32 s14, s13, 0x1100
	s_add_i32 s14, s14, 34816
	v_add_u32_e32 v125, s14, v58
	ds_write_b64 v125, v[6:7]
	s_waitcnt vmcnt(10)
	v_cvt_pk_bf16_f32 v8, v152, v153
	v_cvt_pk_bf16_f32 v9, v154, v155
	s_add_i32 s13, s2, 5
	s_and_b32 s13, s13, 7
	s_mul_i32 s14, s13, 0x1100
	s_add_i32 s14, s14, 34816
	v_add_u32_e32 v10, s14, v58
	ds_write_b64 v10, v[8:9]
	s_waitcnt vmcnt(9)
	v_cvt_pk_bf16_f32 v6, v156, v157
	v_cvt_pk_bf16_f32 v7, v158, v159
	s_add_i32 s13, s2, 6
	s_and_b32 s13, s13, 7
	s_mul_i32 s14, s13, 0x1100
	s_add_i32 s14, s14, 34816
	v_add_u32_e32 v125, s14, v58
	ds_write_b64 v125, v[6:7]
	s_waitcnt vmcnt(8)
	v_cvt_pk_bf16_f32 v8, v160, v161
	v_cvt_pk_bf16_f32 v9, v162, v163
	s_add_i32 s13, s2, 7
	s_and_b32 s13, s13, 7
	s_mul_i32 s14, s13, 0x1100
	s_add_i32 s14, s14, 34816
	v_add_u32_e32 v10, s14, v58
	ds_write_b64 v10, v[8:9]
	s_waitcnt lgkmcnt(0)
	s_barrier
	ds_read_b128 v[28:31], v53
	ds_read_b128 v[60:63], v56
	ds_read_b128 v[32:35], v53 offset:64
	ds_read_b128 v[64:67], v56 offset:64
	ds_read_b128 v[36:39], v53 offset:128
	ds_read_b128 v[68:71], v56 offset:128
	ds_read_b128 v[40:43], v53 offset:192
	ds_read_b128 v[72:75], v56 offset:192
	s_waitcnt lgkmcnt(6)
	v_mfma_f32_16x16x32_bf16 v[18:21], v[28:31], v[60:63], 0
	s_waitcnt lgkmcnt(4)
	v_mfma_f32_16x16x32_bf16 v[18:21], v[32:35], v[64:67], v[18:21]
	s_waitcnt lgkmcnt(2)
	v_mfma_f32_16x16x32_bf16 v[18:21], v[36:39], v[68:71], v[18:21]
	s_waitcnt lgkmcnt(0)
	v_mfma_f32_16x16x32_bf16 v[18:21], v[40:43], v[72:75], v[18:21]
	s_nop 7
	v_mul_f32_e32 v18, s44, v18
	v_mul_f32_e32 v19, s44, v19
	v_mul_f32_e32 v20, s44, v20
	v_mul_f32_e32 v21, s44, v21
	v_cvt_pk_bf16_f32 v18, v18, v18
	v_cvt_pk_bf16_f32 v19, v19, v19
	v_cvt_pk_bf16_f32 v20, v20, v20
	v_cvt_pk_bf16_f32 v21, v21, v21
	ds_write_b16 v55, v18
	ds_write_b16 v55, v19 offset:272
	ds_write_b16 v55, v20 offset:544
	ds_write_b16 v55, v21 offset:816
	s_waitcnt lgkmcnt(0)
	s_barrier
	ds_read_b128 v[28:31], v54
	ds_read_b128 v[60:63], v57
	ds_read_b128 v[32:35], v54 offset:64
	ds_read_b128 v[64:67], v57 offset:64
	ds_read_b128 v[36:39], v54 offset:128
	ds_read_b128 v[68:71], v57 offset:128
	ds_read_b128 v[40:43], v54 offset:192
	ds_read_b128 v[72:75], v57 offset:192
	s_waitcnt lgkmcnt(6)
	v_mfma_f32_16x16x32_bf16 v[18:21], v[28:31], v[60:63], 0
	s_waitcnt lgkmcnt(4)
	v_mfma_f32_16x16x32_bf16 v[18:21], v[32:35], v[64:67], v[18:21]
	s_waitcnt lgkmcnt(2)
	v_mfma_f32_16x16x32_bf16 v[18:21], v[36:39], v[68:71], v[18:21]
	s_waitcnt lgkmcnt(0)
	v_mfma_f32_16x16x32_bf16 v[18:21], v[40:43], v[72:75], v[18:21]
	s_load_dwordx2 s[4:5], s[0:1], 0x68
	v_lshl_or_b32 v26, v24, 2, s12
	v_mov_b32_e32 v107, 0
	v_ashrrev_i32_e32 v27, 31, v26
	v_lshlrev_b64 v[28:29], 9, v[26:27]
	s_waitcnt lgkmcnt(0)
	v_lshl_add_u64 v[30:31], s[4:5], 0, v[106:107]
	v_lshl_add_u64 v[28:29], v[30:31], 0, v[28:29]
	v_mul_u32_u24_e32 v24, 0x440, v24
	s_mov_b32 s4, 0x19200
	global_store_dword v[28:29], v18, off sc1
	v_add3_u32 v28, v24, v25, s4
	v_mul_f32_e32 v24, v18, v18
	v_cvt_pk_bf16_f32 v27, v18, s0
	v_cvt_pk_bf16_f32 v24, v24, s0
	ds_write_b16 v28, v27
	ds_write_b16 v28, v24 offset:4352
	v_max3_f32 v27, |v18|, 0, |v19|
	v_or_b32_e32 v24, 1, v26
	v_cvt_pk_bf16_f32 v18, v19, s0
	v_ashrrev_i32_e32 v25, 31, v24
	ds_write_b16 v28, v18 offset:272
	v_mul_f32_e32 v18, v19, v19
	v_lshlrev_b64 v[24:25], 9, v[24:25]
	v_cvt_pk_bf16_f32 v18, v18, s0
	v_lshl_add_u64 v[24:25], v[30:31], 0, v[24:25]
	ds_write_b16 v28, v18 offset:4624
	v_or_b32_e32 v18, 2, v26
	global_store_dword v[24:25], v19, off sc1
	v_ashrrev_i32_e32 v19, 31, v18
	v_lshlrev_b64 v[18:19], 9, v[18:19]
	v_lshl_add_u64 v[18:19], v[30:31], 0, v[18:19]
	global_store_dword v[18:19], v20, off sc1
	v_cvt_pk_bf16_f32 v18, v20, s0
	ds_write_b16 v28, v18 offset:544
	v_mul_f32_e32 v18, v20, v20
	v_cvt_pk_bf16_f32 v18, v18, s0
	ds_write_b16 v28, v18 offset:4896
	v_or_b32_e32 v18, 3, v26
	v_ashrrev_i32_e32 v19, 31, v18
	v_lshlrev_b64 v[18:19], 9, v[18:19]
	v_lshl_add_u64 v[18:19], v[30:31], 0, v[18:19]
	global_store_dword v[18:19], v21, off sc1
	v_cvt_pk_bf16_f32 v18, v21, s0
	ds_write_b16 v28, v18 offset:816
	v_mul_f32_e32 v18, v21, v21
	v_cvt_pk_bf16_f32 v18, v18, s0
	v_max3_f32 v20, v27, |v20|, |v21|
	ds_write_b16 v28, v18 offset:5168
	v_mov_b32_e32 v18, v107
	v_mov_b32_e32 v19, v107
	v_cmp_eq_u32_e32 vcc, 0, v126
	v_mov_b32_dpp v18, v20 quad_perm:[1,0,3,2] row_mask:0xf bank_mask:0xf
	v_max_f32_e32 v18, v18, v18
	v_max_f32_e32 v18, v20, v18
	s_nop 1
	v_mov_b32_dpp v19, v18 quad_perm:[2,3,0,1] row_mask:0xf bank_mask:0xf
	v_max_f32_e32 v19, v19, v19
	v_max_f32_e32 v18, v18, v19
	v_mov_b32_e32 v19, v107
	s_nop 1
	v_mov_b32_dpp v19, v18 row_half_mirror row_mask:0xf bank_mask:0xf
	v_max_f32_e32 v19, v19, v19
	v_max_f32_e32 v18, v18, v19
	v_mov_b32_e32 v19, v107
	s_nop 1
	v_mov_b32_dpp v19, v18 row_mirror row_mask:0xf bank_mask:0xf
	v_max_f32_e32 v19, v19, v19
	v_max_f32_e32 v18, v18, v19
	s_nop 0
	v_readlane_b32 s8, v18, 0
	v_readlane_b32 s9, v18, 16
	v_readlane_b32 s10, v18, 32
	v_readlane_b32 s11, v18, 48
	v_and_b32_e32 v18, 0x7fffffff, v129
	s_nop 1
	v_add_f32_dpp v18, v18, |v129| quad_perm:[1,0,3,2] row_mask:0xf bank_mask:0xf bound_ctrl:1
	s_nop 1
	v_add_f32_dpp v18, v18, v18 quad_perm:[2,3,0,1] row_mask:0xf bank_mask:0xf bound_ctrl:1
	s_nop 1
	v_add_f32_dpp v18, v18, v18 row_half_mirror row_mask:0xf bank_mask:0xf bound_ctrl:1
	s_nop 1
	v_mov_b32_dpp v107, v18 row_mirror row_mask:0xf bank_mask:0xf
	s_and_saveexec_b64 s[4:5], vcc
	s_cbranch_execz .LBB0_27
	v_mov_b32_e32 v19, 0x1d800
	v_lshl_or_b32 v20, v128, 6, v19
	v_add_f32_e32 v19, v18, v107
	v_max_f32_e64 v18, s11, s11
	v_max_f32_e64 v21, s10, s10
	v_max_f32_e32 v18, v21, v18
	v_mov_b32_e32 v21, s9
	v_max3_f32 v18, s8, v21, v18
	ds_write_b64 v20, v[18:19]

.LBB0_40:
	s_cmpk_gt_i32 s2, 0x7f
	s_cbranch_scc1 .Lp_end
	s_waitcnt vmcnt(9)
	v_mov_b32_e32 v44, 0
	v_cmp_ne_u32_e64 s[46:47], 0, v179
	v_cmp_ne_u32_e64 s[48:49], 0, v178
	v_cmp_ne_u32_e64 s[50:51], 0, v177
	v_cmp_ne_u32_e64 s[52:53], 0, v176
	v_addc_co_u32_e64 v44, s[54:55], v44, v44, s[46:47]
	v_addc_co_u32_e64 v44, s[54:55], v44, v44, s[48:49]
	v_addc_co_u32_e64 v44, s[54:55], v44, v44, s[50:51]
	v_addc_co_u32_e64 v44, s[54:55], v44, v44, s[52:53]
	v_cmp_ne_u32_e64 s[46:47], 0, v175
	v_cmp_ne_u32_e64 s[48:49], 0, v174
	v_cmp_ne_u32_e64 s[50:51], 0, v173
	v_cmp_ne_u32_e64 s[52:53], 0, v172
	v_addc_co_u32_e64 v44, s[54:55], v44, v44, s[46:47]
	v_addc_co_u32_e64 v44, s[54:55], v44, v44, s[48:49]
	v_addc_co_u32_e64 v44, s[54:55], v44, v44, s[50:51]
	v_addc_co_u32_e64 v44, s[54:55], v44, v44, s[52:53]
	v_cmp_ne_u32_e64 s[46:47], 0, v171
	v_cmp_ne_u32_e64 s[48:49], 0, v170
	v_cmp_ne_u32_e64 s[50:51], 0, v169
	v_cmp_ne_u32_e64 s[52:53], 0, v168
	v_addc_co_u32_e64 v44, s[54:55], v44, v44, s[46:47]
	v_addc_co_u32_e64 v44, s[54:55], v44, v44, s[48:49]
	v_addc_co_u32_e64 v44, s[54:55], v44, v44, s[50:51]
	v_addc_co_u32_e64 v44, s[54:55], v44, v44, s[52:53]
	v_cmp_ne_u32_e64 s[46:47], 0, v167
	v_cmp_ne_u32_e64 s[48:49], 0, v166
	v_cmp_ne_u32_e64 s[50:51], 0, v165
	v_cmp_ne_u32_e64 s[52:53], 0, v164
	v_addc_co_u32_e64 v44, s[54:55], v44, v44, s[46:47]
	v_addc_co_u32_e64 v44, s[54:55], v44, v44, s[48:49]
	v_addc_co_u32_e64 v44, s[54:55], v44, v44, s[50:51]
	v_addc_co_u32_e64 v44, s[54:55], v44, v44, s[52:53]
	s_waitcnt vmcnt(5)
	v_mov_b32_e32 v45, 0
	v_cmp_ne_u32_e64 s[46:47], 0, v195
	v_cmp_ne_u32_e64 s[48:49], 0, v194
	v_cmp_ne_u32_e64 s[50:51], 0, v193
	v_cmp_ne_u32_e64 s[52:53], 0, v192
	v_addc_co_u32_e64 v45, s[54:55], v45, v45, s[46:47]
	v_addc_co_u32_e64 v45, s[54:55], v45, v45, s[48:49]
	v_addc_co_u32_e64 v45, s[54:55], v45, v45, s[50:51]
	v_addc_co_u32_e64 v45, s[54:55], v45, v45, s[52:53]
	v_cmp_ne_u32_e64 s[46:47], 0, v191
	v_cmp_ne_u32_e64 s[48:49], 0, v190
	v_cmp_ne_u32_e64 s[50:51], 0, v189
	v_cmp_ne_u32_e64 s[52:53], 0, v188
	v_addc_co_u32_e64 v45, s[54:55], v45, v45, s[46:47]
	v_addc_co_u32_e64 v45, s[54:55], v45, v45, s[48:49]
	v_addc_co_u32_e64 v45, s[54:55], v45, v45, s[50:51]
	v_addc_co_u32_e64 v45, s[54:55], v45, v45, s[52:53]
	v_cmp_ne_u32_e64 s[46:47], 0, v187
	v_cmp_ne_u32_e64 s[48:49], 0, v186
	v_cmp_ne_u32_e64 s[50:51], 0, v185
	v_cmp_ne_u32_e64 s[52:53], 0, v184
	v_addc_co_u32_e64 v45, s[54:55], v45, v45, s[46:47]
	v_addc_co_u32_e64 v45, s[54:55], v45, v45, s[48:49]
	v_addc_co_u32_e64 v45, s[54:55], v45, v45, s[50:51]
	v_addc_co_u32_e64 v45, s[54:55], v45, v45, s[52:53]
	v_cmp_ne_u32_e64 s[46:47], 0, v183
	v_cmp_ne_u32_e64 s[48:49], 0, v182
	v_cmp_ne_u32_e64 s[50:51], 0, v181
	v_cmp_ne_u32_e64 s[52:53], 0, v180
	v_addc_co_u32_e64 v45, s[54:55], v45, v45, s[46:47]
	v_addc_co_u32_e64 v45, s[54:55], v45, v45, s[48:49]
	v_addc_co_u32_e64 v45, s[54:55], v45, v45, s[50:51]
	v_addc_co_u32_e64 v45, s[54:55], v45, v45, s[52:53]
	s_lshl_b32 s13, s2, 4
	v_lshl_add_u32 v46, v128, 1, s13
	v_lshlrev_b32_e32 v46, 7, v46
	v_lshl_add_u32 v46, v126, 1, v46
	global_store_short v46, v44, s[36:37] sc1
	global_store_short v46, v45, s[36:37] offset:128 sc1
